# baseline (speedup 1.0000x reference)
_Z16sum_layer_kernelPKfS0_Pf:
	s_load_dwordx4 s[4:7], s[0:1], 0x0
	s_load_dwordx2 s[8:9], s[0:1], 0x10
	v_lshrrev_b32_e32 v42, 6, v0
	v_bfe_u32 v41, v0, 5, 1
	v_and_b32_e32 v40, 31, v0
	v_readfirstlane_b32 s23, v42
	v_and_b32_e32 v43, 7, v0
	v_bfe_u32 v44, v0, 3, 3
	s_lshl_b32 s3, s2, 12
	s_lshl_b32 s19, s2, 7
	s_lshl_b32 s23, s23, 12
	v_lshlrev_b32_e32 v1, 11, v41
	v_lshl_or_b32 v1, v40, 2, v1
	s_mov_b32 m0, s23
	v_lshrrev_b32_e32 v46, 1, v44
	v_xor_b32_e32 v46, v43, v46
	v_lshlrev_b32_e32 v46, 4, v46
	v_lshl_add_u32 v35, v44, 16, v46
	v_lshl_add_u32 v35, v42, 21, v35
	v_add_u32_e32 v35, s19, v35
	v_xor_b32_e32 v86, 64, v35
	s_mov_b32 s20, 0x7fc00
	s_mov_b32 s21, 0xff800
	s_mov_b32 s22, 0x17f400
	s_mov_b32 s14, 0x200000
	s_mov_b32 s15, 0x20000
	v_and_b32_e32 v45, 63, v0
	v_lshlrev_b32_e32 v37, 4, v45
	s_add_u32 s54, s23, 0x4000
	s_waitcnt lgkmcnt(0)
	s_mov_b32 s12, s6
	s_and_b32 s13, s7, 0xffff
	s_and_b32 s5, s5, 0xffff
	s_mov_b32 s6, 0x800000
	s_mov_b32 s7, s15
	s_mov_b32 m0, s54
	s_nop 0
	buffer_load_dwordx4 v37, s[12:15], s3 offen nt lds
	buffer_load_dwordx4 v37, s[12:15], s3 offen offset:1024 nt lds
	buffer_load_dwordx4 v37, s[12:15], s3 offen offset:2048 nt lds
	buffer_load_dwordx4 v37, s[12:15], s3 offen offset:3072 nt lds
	s_cmp_lt_u32 s23, 0x2000
	s_cbranch_scc1 .Lx_loads_now
	s_sleep 10
.Lx_loads_now:
	s_mov_b32 m0, s23
	s_nop 0
	buffer_load_dwordx4 v35, s[4:7], 0 offen nt lds
	buffer_load_dwordx4 v86, s[4:7], s20 offen offset:1024 nt lds
	buffer_load_dwordx4 v35, s[4:7], s21 offen offset:2048 nt lds
	buffer_load_dwordx4 v86, s[4:7], s22 offen offset:3072 nt lds
	v_and_b32_e32 v45, 63, v0
	v_lshlrev_b32_e32 v36, 2, v40
	v_lshl_add_u32 v36, v41, 18, v36
	v_lshl_add_u32 v36, v42, 21, v36
	v_add_u32_e32 v36, s19, v36
	v_bfe_u32 v47, v40, 1, 3
	v_lshlrev_b32_e32 v39, 2, v41
	v_xor_b32_e32 v39, v39, v47
	v_lshlrev_b32_e32 v39, 4, v39
	v_lshl_add_u32 v39, v40, 7, v39
	v_lshl_add_u32 v39, v42, 12, v39
	v_xor_b32_e32 v81, 16, v39
	v_xor_b32_e32 v82, 32, v39
	v_xor_b32_e32 v83, 48, v39
	v_cmp_gt_u32_e32 vcc, 32, v45
	v_mov_b32_e32 v34, 0xc1600000
	v_mov_b32_e32 v84, 0x3fb8aa3b
	v_mov_b32_e32 v85, 0x3f317218
	s_lshl_b32 s24, 1, 16
	s_lshl_b32 s25, 2, 16
	s_lshl_b32 s26, 3, 16
	s_lshl_b32 s27, 8, 16
	s_lshl_b32 s28, 9, 16
	s_lshl_b32 s29, 10, 16
	s_lshl_b32 s30, 11, 16
	s_lshl_b32 s31, 16, 16
	s_lshl_b32 s32, 17, 16
	s_lshl_b32 s33, 18, 16
	s_lshl_b32 s34, 19, 16
	s_lshl_b32 s35, 24, 16
	s_lshl_b32 s36, 25, 16
	s_lshl_b32 s37, 26, 16
	s_lshl_b32 s38, 27, 16
	s_and_b32 s9, s9, 0xffff
	s_mov_b32 s10, s6
	s_mov_b32 s11, s15
	v_lshl_add_u32 v38, v42, 12, v1
	v_add_u32_e32 v38, 0x4000, v38
	v_add_u32_e32 v87, 0x400, v38
	s_waitcnt vmcnt(4)
	ds_read2_b32 v[18:19], v38 offset0:0 offset1:32
	ds_read2_b32 v[20:21], v38 offset0:64 offset1:96
	ds_read2_b32 v[22:23], v38 offset0:128 offset1:160
	ds_read2_b32 v[24:25], v38 offset0:192 offset1:224
	ds_read2_b32 v[26:27], v87 offset0:0 offset1:32
	ds_read2_b32 v[28:29], v87 offset0:64 offset1:96
	ds_read2_b32 v[30:31], v87 offset0:128 offset1:160
	ds_read2_b32 v[32:33], v87 offset0:192 offset1:224
	s_waitcnt lgkmcnt(0)
	v_max3_f32 v48, v18, v19, v20
	v_max3_f32 v50, v21, v22, v23
	v_max3_f32 v48, v48, v24, v25
	v_max3_f32 v50, v50, v26, v27
	v_max3_f32 v48, v48, v28, v29
	v_max3_f32 v50, v50, v30, v31
	v_max3_f32 v48, v48, v32, v33
	v_max_f32_e32 v48, v48, v50
	v_mov_b32_e32 v50, v48
	s_nop 1
	v_permlane32_swap_b32_e32 v48, v50
	v_max_f32_e32 v48, v48, v50
	v_fmamk_f32 v48, v48, 0x3fb8aa3b, v34
	v_pk_fma_f32 v[18:19], v[18:19], v[84:85], v[48:49] op_sel_hi:[1,0,0] neg_lo:[0,0,1] neg_hi:[0,0,1]
	v_exp_f32_e32 v18, v18
	v_exp_f32_e32 v19, v19
	v_pk_fma_f32 v[20:21], v[20:21], v[84:85], v[48:49] op_sel_hi:[1,0,0] neg_lo:[0,0,1] neg_hi:[0,0,1]
	v_exp_f32_e32 v20, v20
	v_exp_f32_e32 v21, v21
	v_pk_fma_f32 v[22:23], v[22:23], v[84:85], v[48:49] op_sel_hi:[1,0,0] neg_lo:[0,0,1] neg_hi:[0,0,1]
	v_exp_f32_e32 v22, v22
	v_exp_f32_e32 v23, v23
	v_pk_fma_f32 v[24:25], v[24:25], v[84:85], v[48:49] op_sel_hi:[1,0,0] neg_lo:[0,0,1] neg_hi:[0,0,1]
	v_exp_f32_e32 v24, v24
	v_exp_f32_e32 v25, v25
	v_pk_fma_f32 v[26:27], v[26:27], v[84:85], v[48:49] op_sel_hi:[1,0,0] neg_lo:[0,0,1] neg_hi:[0,0,1]
	v_exp_f32_e32 v26, v26
	v_exp_f32_e32 v27, v27
	v_pk_fma_f32 v[28:29], v[28:29], v[84:85], v[48:49] op_sel_hi:[1,0,0] neg_lo:[0,0,1] neg_hi:[0,0,1]
	v_exp_f32_e32 v28, v28
	v_exp_f32_e32 v29, v29
	v_pk_fma_f32 v[30:31], v[30:31], v[84:85], v[48:49] op_sel_hi:[1,0,0] neg_lo:[0,0,1] neg_hi:[0,0,1]
	v_exp_f32_e32 v30, v30
	v_exp_f32_e32 v31, v31
	v_pk_fma_f32 v[32:33], v[32:33], v[84:85], v[48:49] op_sel_hi:[1,0,0] neg_lo:[0,0,1] neg_hi:[0,0,1]
	v_exp_f32_e32 v32, v32
	v_exp_f32_e32 v33, v33
	v_pk_add_f32 v[56:57], v[18:19], v[20:21]
	v_pk_add_f32 v[58:59], v[22:23], v[24:25]
	v_pk_add_f32 v[60:61], v[26:27], v[28:29]
	v_pk_add_f32 v[62:63], v[30:31], v[32:33]
	v_pk_add_f32 v[56:57], v[56:57], v[58:59]
	v_pk_add_f32 v[60:61], v[60:61], v[62:63]
	v_pk_add_f32 v[56:57], v[56:57], v[60:61]
	v_add_f32_e32 v50, v56, v57
	v_mov_b32_e32 v51, v50
	s_nop 1
	v_permlane32_swap_b32_e32 v50, v51
	v_add_f32_e32 v50, v50, v51
	v_log_f32_e32 v50, v50
	v_cvt_pk_f16_f32 v40, v18, v19
	v_cvt_pk_f16_f32 v41, v20, v21
	v_cvt_pk_f16_f32 v42, v22, v23
	v_cvt_pk_f16_f32 v43, v24, v25
	v_cvt_pk_f16_f32 v44, v26, v27
	v_cvt_pk_f16_f32 v45, v28, v29
	v_cvt_pk_f16_f32 v46, v30, v31
	v_cvt_pk_f16_f32 v47, v32, v33
	v_add_f32_e32 v50, 0x41600000, v50
	v_mul_f32_e32 v50, 0xbf317218, v50
	v_cndmask_b32_e64 v51, v50, 1.0, vcc
	s_waitcnt vmcnt(0)
	ds_read_b128 v[2:5], v39
	ds_read_b128 v[6:9], v81
	ds_read_b128 v[10:13], v82
	ds_read_b128 v[14:17], v83
	s_waitcnt lgkmcnt(2)
	v_max3_f32 v52, v2, v3, v4
	v_max3_f32 v53, v5, v6, v7
	v_max_f32_e32 v52, v52, v8
	v_max_f32_e32 v53, v53, v9
	s_waitcnt lgkmcnt(0)
	v_max3_f32 v52, v52, v10, v11
	v_max3_f32 v53, v53, v12, v13
	v_max3_f32 v52, v52, v14, v15
	v_max3_f32 v53, v53, v16, v17
	v_max_f32_e32 v52, v52, v53
	v_mov_b32_e32 v53, v52
	s_nop 1
	v_permlane32_swap_b32_e32 v52, v53
	v_max_f32_e32 v52, v52, v53
	v_cndmask_b32_e32 v54, 1.0, v52, vcc
	v_fmamk_f32 v48, v52, 0x3fb8aa3b, v34
	v_pk_fma_f32 v[2:3], v[2:3], v[84:85], v[48:49] op_sel_hi:[1,0,0] neg_lo:[0,0,1] neg_hi:[0,0,1]
	v_mfma_f32_32x32x2_f32 v[64:79], v54, v51, 0
	v_exp_f32_e32 v2, v2
	v_exp_f32_e32 v3, v3
	v_pk_fma_f32 v[4:5], v[4:5], v[84:85], v[48:49] op_sel_hi:[1,0,0] neg_lo:[0,0,1] neg_hi:[0,0,1]
	v_exp_f32_e32 v4, v4
	v_exp_f32_e32 v5, v5
	v_pk_fma_f32 v[6:7], v[6:7], v[84:85], v[48:49] op_sel_hi:[1,0,0] neg_lo:[0,0,1] neg_hi:[0,0,1]
	v_exp_f32_e32 v6, v6
	v_exp_f32_e32 v7, v7
	v_pk_fma_f32 v[8:9], v[8:9], v[84:85], v[48:49] op_sel_hi:[1,0,0] neg_lo:[0,0,1] neg_hi:[0,0,1]
	v_exp_f32_e32 v8, v8
	v_exp_f32_e32 v9, v9
	v_pk_fma_f32 v[10:11], v[10:11], v[84:85], v[48:49] op_sel_hi:[1,0,0] neg_lo:[0,0,1] neg_hi:[0,0,1]
	v_exp_f32_e32 v10, v10
	v_cvt_pk_f16_f32 v56, v2, v3
	v_cvt_pk_f16_f32 v57, v4, v5
	v_cvt_pk_f16_f32 v58, v6, v7
	v_cvt_pk_f16_f32 v59, v8, v9
	v_exp_f32_e32 v11, v11
	v_pk_fma_f32 v[12:13], v[12:13], v[84:85], v[48:49] op_sel_hi:[1,0,0] neg_lo:[0,0,1] neg_hi:[0,0,1]
	v_exp_f32_e32 v12, v12
	v_mfma_f32_32x32x16_f16 v[18:33], v[56:59], v[40:43], 0
	v_exp_f32_e32 v13, v13
	v_pk_fma_f32 v[14:15], v[14:15], v[84:85], v[48:49] op_sel_hi:[1,0,0] neg_lo:[0,0,1] neg_hi:[0,0,1]
	v_exp_f32_e32 v14, v14
	v_exp_f32_e32 v15, v15
	v_pk_fma_f32 v[16:17], v[16:17], v[84:85], v[48:49] op_sel_hi:[1,0,0] neg_lo:[0,0,1] neg_hi:[0,0,1]
	v_exp_f32_e32 v16, v16
	v_exp_f32_e32 v17, v17
	v_cvt_pk_f16_f32 v60, v10, v11
	v_cvt_pk_f16_f32 v61, v12, v13
	v_cvt_pk_f16_f32 v62, v14, v15
	v_cvt_pk_f16_f32 v63, v16, v17
	s_nop 1
	v_mfma_f32_32x32x16_f16 v[18:33], v[60:63], v[44:47], v[18:33]
	s_nop 11
	v_log_f32_e32 v18, v18
	v_log_f32_e32 v19, v19
	v_log_f32_e32 v20, v20
	v_log_f32_e32 v21, v21
	v_log_f32_e32 v22, v22
	v_log_f32_e32 v23, v23
	v_pk_fma_f32 v[64:65], v[18:19], v[84:85], v[64:65] op_sel:[0,1,0] op_sel_hi:[1,1,1]
	buffer_store_dword v64, v36, s[8:11], 0 offen
	buffer_store_dword v65, v36, s[8:11], s24 offen
	v_log_f32_e32 v24, v24
	v_log_f32_e32 v25, v25
	v_pk_fma_f32 v[66:67], v[20:21], v[84:85], v[66:67] op_sel:[0,1,0] op_sel_hi:[1,1,1]
	buffer_store_dword v66, v36, s[8:11], s25 offen
	buffer_store_dword v67, v36, s[8:11], s26 offen
	v_log_f32_e32 v26, v26
	v_log_f32_e32 v27, v27
	v_pk_fma_f32 v[68:69], v[22:23], v[84:85], v[68:69] op_sel:[0,1,0] op_sel_hi:[1,1,1]
	buffer_store_dword v68, v36, s[8:11], s27 offen
	buffer_store_dword v69, v36, s[8:11], s28 offen
	v_log_f32_e32 v28, v28
	v_log_f32_e32 v29, v29
	v_pk_fma_f32 v[70:71], v[24:25], v[84:85], v[70:71] op_sel:[0,1,0] op_sel_hi:[1,1,1]
	buffer_store_dword v70, v36, s[8:11], s29 offen
	buffer_store_dword v71, v36, s[8:11], s30 offen
	v_log_f32_e32 v30, v30
	v_log_f32_e32 v31, v31
	v_pk_fma_f32 v[72:73], v[26:27], v[84:85], v[72:73] op_sel:[0,1,0] op_sel_hi:[1,1,1]
	buffer_store_dword v72, v36, s[8:11], s31 offen
	buffer_store_dword v73, v36, s[8:11], s32 offen
	v_log_f32_e32 v32, v32
	v_log_f32_e32 v33, v33
	v_pk_fma_f32 v[74:75], v[28:29], v[84:85], v[74:75] op_sel:[0,1,0] op_sel_hi:[1,1,1]
	buffer_store_dword v74, v36, s[8:11], s33 offen
	buffer_store_dword v75, v36, s[8:11], s34 offen
	v_pk_fma_f32 v[76:77], v[30:31], v[84:85], v[76:77] op_sel:[0,1,0] op_sel_hi:[1,1,1]
	buffer_store_dword v76, v36, s[8:11], s35 offen
	buffer_store_dword v77, v36, s[8:11], s36 offen
	v_pk_fma_f32 v[78:79], v[32:33], v[84:85], v[78:79] op_sel:[0,1,0] op_sel_hi:[1,1,1]
	buffer_store_dword v78, v36, s[8:11], s37 offen
	buffer_store_dword v79, v36, s[8:11], s38 offen
	s_endpgm
